# FINAL phase rewritten so each store writes 8 whole 128-B lines (lane owns 4 cols per 256-col slice, 8x dwordx2 row loads, gain hoisted, next rows prefetched); on top of the v8 epilogue prefetch
# speedup vs baseline: 1.0148x; 1.0051x over previous
; __global__ void __launch_bounds__(NTHR, 2) fwd(Args args) {
;     ...
;     if (IN(PH_FINAL)) {
;         const float* gain = F.in[I_NORM_FINAL];
;         for (int t = gw; t < T; t += 2 * NGW) {
;             v4u hv[2][4]; float s[2] = {0.f, 0.f};
; #pragma unroll
;             for (int q = 0; q < 2; ++q)
; #pragma unroll
;                 for (int j = 0; j < 4; ++j) hv[q][j] = __builtin_nontemporal_load((const v4u*)(H + (size_t)(t + q * NGW) * D + 8 * lane + 512 * j));
.LBB0_1812:
	v_mbcnt_lo_u32_b32 v10, -1, 0
	v_mbcnt_hi_u32_b32 v10, -1, v10
	v_lshlrev_b32_e32 v12, 3, v10
	v_sub_u32_e32 v12, 0, v12
	v_ashrrev_i32_e32 v13, 31, v12
	v_lshl_add_u64 v[0:1], v[0:1], 0, v[12:13]
	v_lshlrev_b32_e32 v12, 4, v10
	v_sub_u32_e32 v12, 0, v12
	v_ashrrev_i32_e32 v13, 31, v12
	v_lshl_add_u64 v[2:3], v[2:3], 0, v[12:13]
	v_lshl_add_u64 v[4:5], v[4:5], 0, v[12:13]
	s_mov_b64 s[6:7], 0x1000
	v_lshl_add_u64 v[6:7], v[2:3], 0, s[6:7]
	global_load_dwordx4 v[100:103], v[2:3], off
	global_load_dwordx4 v[104:107], v[2:3], off offset:1024
	global_load_dwordx4 v[108:111], v[2:3], off offset:2048
	global_load_dwordx4 v[112:115], v[2:3], off offset:3072
	global_load_dwordx4 v[116:119], v[6:7], off
	global_load_dwordx4 v[120:123], v[6:7], off offset:1024
	global_load_dwordx4 v[124:127], v[6:7], off offset:2048
	global_load_dwordx4 v[128:131], v[6:7], off offset:3072
	s_ashr_i32 s5, s30, 31
	s_mov_b32 s4, s30
	s_lshl_b64 s[6:7], s[4:5], 12
	v_lshl_add_u64 v[10:11], v[0:1], 0, s[6:7]
	global_load_dwordx2 v[208:209], v[10:11], off nt
	global_load_dwordx2 v[210:211], v[10:11], off offset:512 nt
	global_load_dwordx2 v[212:213], v[10:11], off offset:1024 nt
	global_load_dwordx2 v[214:215], v[10:11], off offset:1536 nt
	global_load_dwordx2 v[216:217], v[10:11], off offset:2048 nt
	global_load_dwordx2 v[218:219], v[10:11], off offset:2560 nt
	global_load_dwordx2 v[220:221], v[10:11], off offset:3072 nt
	global_load_dwordx2 v[222:223], v[10:11], off offset:3584 nt
	s_add_i32 s4, s38, s30
	s_ashr_i32 s5, s4, 31
	s_lshl_b64 s[6:7], s[4:5], 12
	v_lshl_add_u64 v[10:11], v[0:1], 0, s[6:7]
	global_load_dwordx2 v[224:225], v[10:11], off nt
	global_load_dwordx2 v[226:227], v[10:11], off offset:512 nt
	global_load_dwordx2 v[228:229], v[10:11], off offset:1024 nt
	global_load_dwordx2 v[230:231], v[10:11], off offset:1536 nt
	global_load_dwordx2 v[232:233], v[10:11], off offset:2048 nt
	global_load_dwordx2 v[234:235], v[10:11], off offset:2560 nt
	global_load_dwordx2 v[236:237], v[10:11], off offset:3072 nt
	global_load_dwordx2 v[238:239], v[10:11], off offset:3584 nt
	s_waitcnt vmcnt(0)
.Lfin_loop:
	v_mov_b32_e32 v176, v208
	v_mov_b32_e32 v177, v209
	v_mov_b32_e32 v178, v210
	v_mov_b32_e32 v179, v211
	v_mov_b32_e32 v180, v212
	v_mov_b32_e32 v181, v213
	v_mov_b32_e32 v182, v214
	v_mov_b32_e32 v183, v215
	v_mov_b32_e32 v184, v216
	v_mov_b32_e32 v185, v217
	v_mov_b32_e32 v186, v218
	v_mov_b32_e32 v187, v219
	v_mov_b32_e32 v188, v220
	v_mov_b32_e32 v189, v221
	v_mov_b32_e32 v190, v222
	v_mov_b32_e32 v191, v223
	v_mov_b32_e32 v192, v224
	v_mov_b32_e32 v193, v225
	v_mov_b32_e32 v194, v226
	v_mov_b32_e32 v195, v227
	v_mov_b32_e32 v196, v228
	v_mov_b32_e32 v197, v229
	v_mov_b32_e32 v198, v230
	v_mov_b32_e32 v199, v231
	v_mov_b32_e32 v200, v232
	v_mov_b32_e32 v201, v233
	v_mov_b32_e32 v202, v234
	v_mov_b32_e32 v203, v235
	v_mov_b32_e32 v204, v236
	v_mov_b32_e32 v205, v237
	v_mov_b32_e32 v206, v238
	v_mov_b32_e32 v207, v239
	s_add_i32 s0, s30, s2
	s_cmp_lt_i32 s0, 0x8000
	s_cbranch_scc0 .Lfin_noload
	s_ashr_i32 s5, s0, 31
	s_mov_b32 s4, s0
	s_lshl_b64 s[6:7], s[4:5], 12
	v_lshl_add_u64 v[10:11], v[0:1], 0, s[6:7]
	global_load_dwordx2 v[208:209], v[10:11], off nt
	global_load_dwordx2 v[210:211], v[10:11], off offset:512 nt
	global_load_dwordx2 v[212:213], v[10:11], off offset:1024 nt
	global_load_dwordx2 v[214:215], v[10:11], off offset:1536 nt
	global_load_dwordx2 v[216:217], v[10:11], off offset:2048 nt
	global_load_dwordx2 v[218:219], v[10:11], off offset:2560 nt
	global_load_dwordx2 v[220:221], v[10:11], off offset:3072 nt
	global_load_dwordx2 v[222:223], v[10:11], off offset:3584 nt
	s_add_i32 s4, s38, s0
	s_ashr_i32 s5, s4, 31
	s_lshl_b64 s[6:7], s[4:5], 12
	v_lshl_add_u64 v[10:11], v[0:1], 0, s[6:7]
	global_load_dwordx2 v[224:225], v[10:11], off nt
	global_load_dwordx2 v[226:227], v[10:11], off offset:512 nt
	global_load_dwordx2 v[228:229], v[10:11], off offset:1024 nt
	global_load_dwordx2 v[230:231], v[10:11], off offset:1536 nt
	global_load_dwordx2 v[232:233], v[10:11], off offset:2048 nt
	global_load_dwordx2 v[234:235], v[10:11], off offset:2560 nt
	global_load_dwordx2 v[236:237], v[10:11], off offset:3072 nt
	global_load_dwordx2 v[238:239], v[10:11], off offset:3584 nt
; __device__ __forceinline__ void unpack8bf(const v4u o, float* v) { v[0] = bflo(o.x); v[1] = bfhi(o.x); v[2] = bflo(o.y); v[3] = bfhi(o.y); v[4] = bflo(o.z); v[5] = bfhi(o.z); v[6] = bflo(o.w); v[7] = bfhi(o.w); }
; __device__ __forceinline__ float wave_sum(float v) {
; #pragma unroll
;     for (int o = 1; o < 64; o <<= 1) v += __shfl_xor(v, o);
;     return v;
; }
; __global__ void __launch_bounds__(NTHR, 2) fwd(Args args) {
;     ...
; #pragma unroll
;             for (int q = 0; q < 2; ++q)
; #pragma unroll
;                 for (int j = 0; j < 4; ++j) { float a[8]; unpack8bf(hv[q][j], a);
; #pragma unroll
;                     for (int i = 0; i < 8; ++i) s[q] += a[i] * a[i]; }
; #pragma unroll
;             for (int q = 0; q < 2; ++q) { const float rstd = __builtin_amdgcn_rsqf(wave_sum(s[q]) * (1.f / D) + EPS); float* orow = F.out + (size_t)(t + q * NGW) * D + 8 * lane;
.Lfin_noload:
	v_lshlrev_b32_e32 v28, 16, v176
	v_and_b32_e32 v29, 0xffff0000, v176
	v_lshlrev_b32_e32 v30, 16, v177
	v_and_b32_e32 v31, 0xffff0000, v177
	v_lshlrev_b32_e32 v32, 16, v178
	v_and_b32_e32 v33, 0xffff0000, v178
	v_lshlrev_b32_e32 v34, 16, v179
	v_and_b32_e32 v35, 0xffff0000, v179
	v_lshlrev_b32_e32 v36, 16, v180
	v_and_b32_e32 v37, 0xffff0000, v180
	v_lshlrev_b32_e32 v38, 16, v181
	v_and_b32_e32 v39, 0xffff0000, v181
	v_lshlrev_b32_e32 v40, 16, v182
	v_and_b32_e32 v41, 0xffff0000, v182
	v_lshlrev_b32_e32 v42, 16, v183
	v_and_b32_e32 v43, 0xffff0000, v183
	v_lshlrev_b32_e32 v44, 16, v184
	v_and_b32_e32 v45, 0xffff0000, v184
	v_lshlrev_b32_e32 v46, 16, v185
	v_and_b32_e32 v47, 0xffff0000, v185
	v_lshlrev_b32_e32 v48, 16, v186
	v_and_b32_e32 v49, 0xffff0000, v186
	v_lshlrev_b32_e32 v50, 16, v187
	v_and_b32_e32 v51, 0xffff0000, v187
	v_lshlrev_b32_e32 v52, 16, v188
	v_and_b32_e32 v53, 0xffff0000, v188
	v_lshlrev_b32_e32 v54, 16, v189
	v_and_b32_e32 v55, 0xffff0000, v189
	v_lshlrev_b32_e32 v56, 16, v190
	v_and_b32_e32 v57, 0xffff0000, v190
	v_lshlrev_b32_e32 v58, 16, v191
	v_and_b32_e32 v59, 0xffff0000, v191
	v_mul_f32_e32 v240, v28, v28
	v_mul_f32_e32 v241, v29, v29
	v_mul_f32_e32 v242, v30, v30
	v_mul_f32_e32 v243, v31, v31
	v_fmac_f32_e32 v240, v32, v32
	v_fmac_f32_e32 v241, v33, v33
	v_fmac_f32_e32 v242, v34, v34
	v_fmac_f32_e32 v243, v35, v35
	v_fmac_f32_e32 v240, v36, v36
	v_fmac_f32_e32 v241, v37, v37
	v_fmac_f32_e32 v242, v38, v38
	v_fmac_f32_e32 v243, v39, v39
	v_fmac_f32_e32 v240, v40, v40
	v_fmac_f32_e32 v241, v41, v41
	v_fmac_f32_e32 v242, v42, v42
	v_fmac_f32_e32 v243, v43, v43
	v_fmac_f32_e32 v240, v44, v44
	v_fmac_f32_e32 v241, v45, v45
	v_fmac_f32_e32 v242, v46, v46
	v_fmac_f32_e32 v243, v47, v47
	v_fmac_f32_e32 v240, v48, v48
	v_fmac_f32_e32 v241, v49, v49
	v_fmac_f32_e32 v242, v50, v50
	v_fmac_f32_e32 v243, v51, v51
	v_fmac_f32_e32 v240, v52, v52
	v_fmac_f32_e32 v241, v53, v53
	v_fmac_f32_e32 v242, v54, v54
	v_fmac_f32_e32 v243, v55, v55
	v_fmac_f32_e32 v240, v56, v56
	v_fmac_f32_e32 v241, v57, v57
	v_fmac_f32_e32 v242, v58, v58
	v_fmac_f32_e32 v243, v59, v59
	v_add_f32_e32 v240, v240, v241
	v_add_f32_e32 v242, v242, v243
	v_add_f32_e32 v92, v240, v242
	v_lshlrev_b32_e32 v60, 16, v192
	v_and_b32_e32 v61, 0xffff0000, v192
	v_lshlrev_b32_e32 v62, 16, v193
	v_and_b32_e32 v63, 0xffff0000, v193
	v_lshlrev_b32_e32 v64, 16, v194
	v_and_b32_e32 v65, 0xffff0000, v194
	v_lshlrev_b32_e32 v66, 16, v195
	v_and_b32_e32 v67, 0xffff0000, v195
	v_lshlrev_b32_e32 v68, 16, v196
	v_and_b32_e32 v69, 0xffff0000, v196
	v_lshlrev_b32_e32 v70, 16, v197
	v_and_b32_e32 v71, 0xffff0000, v197
	v_lshlrev_b32_e32 v72, 16, v198
	v_and_b32_e32 v73, 0xffff0000, v198
	v_lshlrev_b32_e32 v74, 16, v199
	v_and_b32_e32 v75, 0xffff0000, v199
	v_lshlrev_b32_e32 v76, 16, v200
	v_and_b32_e32 v77, 0xffff0000, v200
	v_lshlrev_b32_e32 v78, 16, v201
	v_and_b32_e32 v79, 0xffff0000, v201
	v_lshlrev_b32_e32 v80, 16, v202
	v_and_b32_e32 v81, 0xffff0000, v202
	v_lshlrev_b32_e32 v82, 16, v203
	v_and_b32_e32 v83, 0xffff0000, v203
	v_lshlrev_b32_e32 v84, 16, v204
	v_and_b32_e32 v85, 0xffff0000, v204
	v_lshlrev_b32_e32 v86, 16, v205
	v_and_b32_e32 v87, 0xffff0000, v205
	v_lshlrev_b32_e32 v88, 16, v206
	v_and_b32_e32 v89, 0xffff0000, v206
	v_lshlrev_b32_e32 v90, 16, v207
	v_and_b32_e32 v91, 0xffff0000, v207
	v_mul_f32_e32 v240, v60, v60
	v_mul_f32_e32 v241, v61, v61
	v_mul_f32_e32 v242, v62, v62
	v_mul_f32_e32 v243, v63, v63
	v_fmac_f32_e32 v240, v64, v64
	v_fmac_f32_e32 v241, v65, v65
	v_fmac_f32_e32 v242, v66, v66
	v_fmac_f32_e32 v243, v67, v67
	v_fmac_f32_e32 v240, v68, v68
	v_fmac_f32_e32 v241, v69, v69
	v_fmac_f32_e32 v242, v70, v70
	v_fmac_f32_e32 v243, v71, v71
	v_fmac_f32_e32 v240, v72, v72
	v_fmac_f32_e32 v241, v73, v73
	v_fmac_f32_e32 v242, v74, v74
	v_fmac_f32_e32 v243, v75, v75
	v_fmac_f32_e32 v240, v76, v76
	v_fmac_f32_e32 v241, v77, v77
	v_fmac_f32_e32 v242, v78, v78
	v_fmac_f32_e32 v243, v79, v79
	v_fmac_f32_e32 v240, v80, v80
	v_fmac_f32_e32 v241, v81, v81
	v_fmac_f32_e32 v242, v82, v82
	v_fmac_f32_e32 v243, v83, v83
	v_fmac_f32_e32 v240, v84, v84
	v_fmac_f32_e32 v241, v85, v85
	v_fmac_f32_e32 v242, v86, v86
	v_fmac_f32_e32 v243, v87, v87
	v_fmac_f32_e32 v240, v88, v88
	v_fmac_f32_e32 v241, v89, v89
	v_fmac_f32_e32 v242, v90, v90
	v_fmac_f32_e32 v243, v91, v91
	v_add_f32_e32 v240, v240, v241
	v_add_f32_e32 v242, v242, v243
	v_add_f32_e32 v93, v240, v242
	ds_bpermute_b32 v94, v20, v92
	ds_bpermute_b32 v95, v20, v93
	s_waitcnt lgkmcnt(0)
	v_add_f32_e32 v92, v92, v94
	v_add_f32_e32 v93, v93, v95
	ds_bpermute_b32 v94, v21, v92
	ds_bpermute_b32 v95, v21, v93
	s_waitcnt lgkmcnt(0)
	v_add_f32_e32 v92, v92, v94
	v_add_f32_e32 v93, v93, v95
	ds_bpermute_b32 v94, v22, v92
	ds_bpermute_b32 v95, v22, v93
	s_waitcnt lgkmcnt(0)
	v_add_f32_e32 v92, v92, v94
	v_add_f32_e32 v93, v93, v95
	ds_bpermute_b32 v94, v23, v92
	ds_bpermute_b32 v95, v23, v93
	s_waitcnt lgkmcnt(0)
	v_add_f32_e32 v92, v92, v94
	v_add_f32_e32 v93, v93, v95
	ds_bpermute_b32 v94, v24, v92
	ds_bpermute_b32 v95, v24, v93
	s_waitcnt lgkmcnt(0)
	v_add_f32_e32 v92, v92, v94
	v_add_f32_e32 v93, v93, v95
	ds_bpermute_b32 v94, v25, v92
	ds_bpermute_b32 v95, v25, v93
	s_waitcnt lgkmcnt(0)
; __device__ __forceinline__ void unpack8bf(const v4u o, float* v) { v[0] = bflo(o.x); v[1] = bfhi(o.x); v[2] = bflo(o.y); v[3] = bfhi(o.y); v[4] = bflo(o.z); v[5] = bfhi(o.z); v[6] = bflo(o.w); v[7] = bfhi(o.w); }
; __global__ void __launch_bounds__(NTHR, 2) fwd(Args args) {
;     ...
;             for (int q = 0; q < 2; ++q) { const float rstd = __builtin_amdgcn_rsqf(wave_sum(s[q]) * (1.f / D) + EPS); float* orow = F.out + (size_t)(t + q * NGW) * D + 8 * lane;
; #pragma unroll
;                 for (int j = 0; j < 4; ++j) { const f32x4 g0 = *(const f32x4*)(gain + 512 * j + 8 * lane), g1 = *(const f32x4*)(gain + 512 * j + 8 * lane + 4); float a[8]; unpack8bf(hv[q][j], a);
;                     __builtin_nontemporal_store((f32x4){a[0] * rstd * g0[0], a[1] * rstd * g0[1], a[2] * rstd * g0[2], a[3] * rstd * g0[3]}, (f32x4*)(orow + 512 * j));
;                     __builtin_nontemporal_store((f32x4){a[4] * rstd * g1[0], a[5] * rstd * g1[1], a[6] * rstd * g1[2], a[7] * rstd * g1[3]}, (f32x4*)(orow + 512 * j + 4)); } }
;         }
	v_add_f32_e32 v92, v92, v94
	v_add_f32_e32 v93, v93, v95
	v_fmamk_f32 v92, v92, 0x3a000000, v26
	v_fmamk_f32 v93, v93, 0x3a000000, v26
	v_rsq_f32_e32 v96, v92
	v_rsq_f32_e32 v97, v93
	s_nop 0
	s_ashr_i32 s5, s30, 31
	s_mov_b32 s4, s30
	s_lshl_b64 s[6:7], s[4:5], 13
	v_lshl_add_u64 v[12:13], v[4:5], 0, s[6:7]
	s_add_i32 s4, s38, s30
	s_ashr_i32 s5, s4, 31
	s_lshl_b64 s[6:7], s[4:5], 13
	v_lshl_add_u64 v[14:15], v[4:5], 0, s[6:7]
	v_add_co_u32_e32 v16, vcc, 0x1000, v12
	s_nop 1
	v_addc_co_u32_e32 v17, vcc, 0, v13, vcc
	v_add_co_u32_e32 v18, vcc, 0x1000, v14
	s_nop 1
	v_addc_co_u32_e32 v19, vcc, 0, v15, vcc
	v_mul_f32_e32 v28, v96, v28
	v_mul_f32_e32 v29, v96, v29
	v_mul_f32_e32 v30, v96, v30
	v_mul_f32_e32 v31, v96, v31
	v_mul_f32_e32 v28, v100, v28
	v_mul_f32_e32 v29, v101, v29
	v_mul_f32_e32 v30, v102, v30
	v_mul_f32_e32 v31, v103, v31
	global_store_dwordx4 v[12:13], v[28:31], off nt
	v_mul_f32_e32 v32, v96, v32
	v_mul_f32_e32 v33, v96, v33
	v_mul_f32_e32 v34, v96, v34
	v_mul_f32_e32 v35, v96, v35
	v_mul_f32_e32 v32, v104, v32
	v_mul_f32_e32 v33, v105, v33
	v_mul_f32_e32 v34, v106, v34
	v_mul_f32_e32 v35, v107, v35
	global_store_dwordx4 v[12:13], v[32:35], off offset:1024 nt
	v_mul_f32_e32 v36, v96, v36
	v_mul_f32_e32 v37, v96, v37
	v_mul_f32_e32 v38, v96, v38
	v_mul_f32_e32 v39, v96, v39
	v_mul_f32_e32 v36, v108, v36
	v_mul_f32_e32 v37, v109, v37
	v_mul_f32_e32 v38, v110, v38
	v_mul_f32_e32 v39, v111, v39
	global_store_dwordx4 v[12:13], v[36:39], off offset:2048 nt
	v_mul_f32_e32 v40, v96, v40
	v_mul_f32_e32 v41, v96, v41
	v_mul_f32_e32 v42, v96, v42
	v_mul_f32_e32 v43, v96, v43
	v_mul_f32_e32 v40, v112, v40
	v_mul_f32_e32 v41, v113, v41
	v_mul_f32_e32 v42, v114, v42
	v_mul_f32_e32 v43, v115, v43
	global_store_dwordx4 v[12:13], v[40:43], off offset:3072 nt
	v_mul_f32_e32 v44, v96, v44
	v_mul_f32_e32 v45, v96, v45
	v_mul_f32_e32 v46, v96, v46
	v_mul_f32_e32 v47, v96, v47
	v_mul_f32_e32 v44, v116, v44
	v_mul_f32_e32 v45, v117, v45
	v_mul_f32_e32 v46, v118, v46
	v_mul_f32_e32 v47, v119, v47
	global_store_dwordx4 v[16:17], v[44:47], off nt
	v_mul_f32_e32 v48, v96, v48
	v_mul_f32_e32 v49, v96, v49
	v_mul_f32_e32 v50, v96, v50
	v_mul_f32_e32 v51, v96, v51
	v_mul_f32_e32 v48, v120, v48
	v_mul_f32_e32 v49, v121, v49
	v_mul_f32_e32 v50, v122, v50
	v_mul_f32_e32 v51, v123, v51
	global_store_dwordx4 v[16:17], v[48:51], off offset:1024 nt
	v_mul_f32_e32 v52, v96, v52
	v_mul_f32_e32 v53, v96, v53
	v_mul_f32_e32 v54, v96, v54
	v_mul_f32_e32 v55, v96, v55
	v_mul_f32_e32 v52, v124, v52
	v_mul_f32_e32 v53, v125, v53
	v_mul_f32_e32 v54, v126, v54
	v_mul_f32_e32 v55, v127, v55
	global_store_dwordx4 v[16:17], v[52:55], off offset:2048 nt
	v_mul_f32_e32 v56, v96, v56
	v_mul_f32_e32 v57, v96, v57
	v_mul_f32_e32 v58, v96, v58
	v_mul_f32_e32 v59, v96, v59
	v_mul_f32_e32 v56, v128, v56
	v_mul_f32_e32 v57, v129, v57
	v_mul_f32_e32 v58, v130, v58
	v_mul_f32_e32 v59, v131, v59
	global_store_dwordx4 v[16:17], v[56:59], off offset:3072 nt
	v_mul_f32_e32 v60, v97, v60
	v_mul_f32_e32 v61, v97, v61
	v_mul_f32_e32 v62, v97, v62
	v_mul_f32_e32 v63, v97, v63
	v_mul_f32_e32 v60, v100, v60
	v_mul_f32_e32 v61, v101, v61
	v_mul_f32_e32 v62, v102, v62
	v_mul_f32_e32 v63, v103, v63
	global_store_dwordx4 v[14:15], v[60:63], off nt
	v_mul_f32_e32 v64, v97, v64
	v_mul_f32_e32 v65, v97, v65
	v_mul_f32_e32 v66, v97, v66
	v_mul_f32_e32 v67, v97, v67
	v_mul_f32_e32 v64, v104, v64
	v_mul_f32_e32 v65, v105, v65
	v_mul_f32_e32 v66, v106, v66
	v_mul_f32_e32 v67, v107, v67
	global_store_dwordx4 v[14:15], v[64:67], off offset:1024 nt
	v_mul_f32_e32 v68, v97, v68
	v_mul_f32_e32 v69, v97, v69
	v_mul_f32_e32 v70, v97, v70
	v_mul_f32_e32 v71, v97, v71
	v_mul_f32_e32 v68, v108, v68
	v_mul_f32_e32 v69, v109, v69
	v_mul_f32_e32 v70, v110, v70
	v_mul_f32_e32 v71, v111, v71
	global_store_dwordx4 v[14:15], v[68:71], off offset:2048 nt
	v_mul_f32_e32 v72, v97, v72
	v_mul_f32_e32 v73, v97, v73
	v_mul_f32_e32 v74, v97, v74
	v_mul_f32_e32 v75, v97, v75
	v_mul_f32_e32 v72, v112, v72
	v_mul_f32_e32 v73, v113, v73
	v_mul_f32_e32 v74, v114, v74
	v_mul_f32_e32 v75, v115, v75
	global_store_dwordx4 v[14:15], v[72:75], off offset:3072 nt
	v_mul_f32_e32 v76, v97, v76
	v_mul_f32_e32 v77, v97, v77
	v_mul_f32_e32 v78, v97, v78
	v_mul_f32_e32 v79, v97, v79
	v_mul_f32_e32 v76, v116, v76
	v_mul_f32_e32 v77, v117, v77
	v_mul_f32_e32 v78, v118, v78
	v_mul_f32_e32 v79, v119, v79
	global_store_dwordx4 v[18:19], v[76:79], off nt
	v_mul_f32_e32 v80, v97, v80
	v_mul_f32_e32 v81, v97, v81
	v_mul_f32_e32 v82, v97, v82
	v_mul_f32_e32 v83, v97, v83
	v_mul_f32_e32 v80, v120, v80
	v_mul_f32_e32 v81, v121, v81
	v_mul_f32_e32 v82, v122, v82
	v_mul_f32_e32 v83, v123, v83
	global_store_dwordx4 v[18:19], v[80:83], off offset:1024 nt
	v_mul_f32_e32 v84, v97, v84
	v_mul_f32_e32 v85, v97, v85
	v_mul_f32_e32 v86, v97, v86
	v_mul_f32_e32 v87, v97, v87
	v_mul_f32_e32 v84, v124, v84
	v_mul_f32_e32 v85, v125, v85
	v_mul_f32_e32 v86, v126, v86
	v_mul_f32_e32 v87, v127, v87
	global_store_dwordx4 v[18:19], v[84:87], off offset:2048 nt
	v_mul_f32_e32 v88, v97, v88
	v_mul_f32_e32 v89, v97, v89
	v_mul_f32_e32 v90, v97, v90
	v_mul_f32_e32 v91, v97, v91
	v_mul_f32_e32 v88, v128, v88
	v_mul_f32_e32 v89, v129, v89
	v_mul_f32_e32 v90, v130, v90
	v_mul_f32_e32 v91, v131, v91
	global_store_dwordx4 v[18:19], v[88:91], off offset:3072 nt
	s_add_i32 s30, s30, s2
	s_cmp_lt_i32 s30, 0x8000
	s_cbranch_scc0 .Lfin_done
	s_waitcnt vmcnt(16)
	s_branch .Lfin_loop
.Lfin_done:
.LBB0_1813:
	s_endpgm
